# P1 norm loop: next-row prefetch no longer serialised (loads land in holding registers, false vmcnt waits for pre-loop weight loads removed, bias load hoisted)
# baseline (speedup 1.0000x reference)
.LBB0_58:
	v_readlane_b32 s10, v255, 15
	s_cmp_lg_u32 s10, 0
	v_readlane_b32 s8, v255, 19
	s_cselect_b64 s[4:5], -1, 0
	v_readlane_b32 s9, v255, 20
	s_and_b64 s[4:5], s[4:5], s[8:9]
	s_add_u32 s8, s16, 0x5c00000
	s_addc_u32 s9, s17, 0
	s_and_b64 s[4:5], s[4:5], exec
	s_cselect_b32 s5, s9, 0
	s_cselect_b32 s4, s8, 0
	s_cmp_lg_u64 s[4:5], 0
	s_cselect_b64 s[22:23], -1, 0
	s_lshl_b32 s52, s10, 3
	s_lshl_b64 s[8:9], s[52:53], 2
	s_waitcnt lgkmcnt(0)
	s_add_u32 s24, s6, s8
	v_and_b32_e32 v20, 4, v22
	v_readlane_b32 s11, v255, 16
	s_addc_u32 s25, s7, s9
	v_cmp_eq_u32_e64 s[8:9], 0, v20
	v_and_b32_e32 v20, 2, v22
	v_cmp_eq_u32_e64 s[10:11], 0, v20
	v_and_b32_e32 v20, 1, v22
	v_cmp_ne_u32_e64 s[6:7], 0, v19
	v_cmp_eq_u32_e64 s[12:13], 0, v20
	v_cmp_gt_u32_e64 s[14:15], 8, v19
	v_lshlrev_b32_e32 v20, 2, v19
	v_and_b32_e32 v19, 64, v234
	v_add_u32_e32 v19, 64, v19
	v_xor_b32_e32 v22, 1, v234
	v_cmp_lt_i32_e32 vcc, v22, v19
	v_mov_b32_e32 v21, v1
	v_lshl_add_u64 v[206:207], s[24:25], 0, v[20:21]
	v_cndmask_b32_e32 v22, v234, v22, vcc
	v_lshlrev_b32_e32 v214, 2, v22
	v_xor_b32_e32 v22, 2, v234
	v_cmp_lt_i32_e32 vcc, v22, v19
	v_lshl_add_u64 v[20:21], s[16:17], 0, v[20:21]
	s_mov_b64 s[24:25], 0x100000
	v_cndmask_b32_e32 v22, v234, v22, vcc
	v_lshlrev_b32_e32 v215, 2, v22
	v_xor_b32_e32 v22, 4, v234
	v_cmp_lt_i32_e32 vcc, v22, v19
	v_lshl_add_u64 v[208:209], v[20:21], 0, s[24:25]
	s_mov_b64 s[24:25], 0x35600000
	v_cndmask_b32_e32 v22, v234, v22, vcc
	v_lshlrev_b32_e32 v216, 2, v22
	v_xor_b32_e32 v22, 8, v234
	v_cmp_lt_i32_e32 vcc, v22, v19
	v_readlane_b32 s30, v252, 10
	v_lshl_add_u64 v[210:211], v[20:21], 0, s[24:25]
	v_cndmask_b32_e32 v22, v234, v22, vcc
	v_lshlrev_b32_e32 v217, 2, v22
	v_xor_b32_e32 v22, 16, v234
	v_cmp_lt_i32_e32 vcc, v22, v19
	v_readlane_b32 s31, v252, 11
	s_add_u32 s24, s16, s30
	v_cndmask_b32_e32 v22, v234, v22, vcc
	s_addc_u32 s25, s17, s31
	v_readlane_b32 s26, v254, 23
	v_lshlrev_b32_e32 v218, 2, v22
	v_xor_b32_e32 v22, 32, v234
	s_add_u32 s26, s16, s26
	v_readlane_b32 s27, v254, 24
	v_cmp_lt_i32_e32 vcc, v22, v19
	s_addc_u32 s27, s17, s27
	v_readlane_b32 s34, v254, 25
	v_cndmask_b32_e32 v19, v234, v22, vcc
	v_readlane_b32 s35, v254, 26
	s_add_u32 s28, s28, s34
	v_lshlrev_b32_e32 v219, 2, v19
	s_addc_u32 s29, s29, s35
	v_mov_b32_e32 v19, v1
	v_lshl_add_u64 v[212:213], s[28:29], 0, v[18:19]
	s_add_u32 s28, s4, s30
	s_addc_u32 s29, s5, s31
	v_readlane_b32 s4, v254, 38
	v_readlane_b32 s5, v254, 39
	s_add_u32 s30, s16, s4
	s_mov_b64 s[20:21], 0
	s_addc_u32 s31, s17, s5
	s_mov_b32 s36, s50
	s_mov_b64 vcc, exec
	s_mov_b64 exec, s[14:15]
	global_load_dword v240, v[206:207], off
	s_mov_b64 exec, vcc
	s_waitcnt vmcnt(0)
	s_branch .LBB0_60

.LBB0_63:
	s_add_i32 s33, s36, s42
	s_cmpk_gt_i32 s33, 0x7fff
	s_cselect_b64 s[34:35], -1, 0
	s_and_b64 vcc, exec, s[34:35]
	s_cbranch_vccnz .LBB0_68
	s_and_b64 vcc, exec, s[16:17]
	s_cbranch_vccnz .LBB0_79
	global_load_dwordx4 v[2:5], v[212:213], off offset:-2048
	global_load_dwordx4 v[6:9], v[212:213], off offset:-1024
	global_load_dwordx4 v[10:13], v[212:213], off
	global_load_dwordx4 v[14:17], v[212:213], off offset:1024
	s_branch .LBB0_68
.LBB0_66:

	v_lshl_add_u64 v[178:179], s[30:31], 0, v[0:1]
	v_add_co_u32_e32 v178, vcc, 0x1c00000, v178
	v_mov_b64_e32 v[184:185], v[12:13]
	s_nop 0
	v_addc_co_u32_e32 v179, vcc, 0, v179, vcc
	global_load_dwordx2 v[198:199], v[178:179], off
	global_load_dwordx2 v[200:201], v[178:179], off offset:512
	global_load_dwordx2 v[202:203], v[178:179], off offset:1024
	global_load_dwordx2 v[204:205], v[178:179], off offset:1536
	v_mov_b64_e32 v[180:181], v[16:17]
	v_mov_b64_e32 v[188:189], v[8:9]
	v_mov_b64_e32 v[192:193], v[4:5]
	v_mov_b64_e32 v[178:179], v[14:15]
	v_mov_b64_e32 v[182:183], v[10:11]
	v_mov_b64_e32 v[186:187], v[6:7]
	v_mov_b64_e32 v[190:191], v[2:3]
.LBB0_67:

	v_mov_b64_e32 v[2:3], v[190:191]

	v_mov_b64_e32 v[6:7], v[186:187]

	v_mov_b64_e32 v[10:11], v[182:183]

	v_mov_b64_e32 v[14:15], v[178:179]
	v_mov_b64_e32 v[4:5], v[192:193]
	v_mov_b64_e32 v[8:9], v[188:189]
	v_mov_b64_e32 v[12:13], v[184:185]
	v_mov_b64_e32 v[16:17], v[180:181]

.LBB0_72:
	s_waitcnt lgkmcnt(0)
	v_pk_mul_f32 v[182:183], v[20:21], v[20:21]
	v_pk_mul_f32 v[184:185], v[18:19], v[18:19]
	v_pk_mul_f32 v[178:179], v[24:25], v[24:25]
	v_pk_mul_f32 v[180:181], v[22:23], v[22:23]
	v_pk_mov_b32 v[186:187], v[184:185], v[182:183] op_sel:[1,0]
	v_mov_b32_e32 v185, v183
	v_pk_add_f32 v[182:183], v[186:187], v[184:185]
	v_pk_mov_b32 v[184:185], v[180:181], v[178:179] op_sel:[1,0]
	v_mov_b32_e32 v181, v179
	v_pk_add_f32 v[178:179], v[184:185], v[180:181]
	v_pk_add_f32 v[182:183], v[182:183], v[182:183] op_sel_hi:[0,1]
	v_pk_add_f32 v[178:179], v[178:179], v[178:179] op_sel_hi:[0,1]
	v_mul_f32_e32 v178, v26, v26
	v_pk_fma_f32 v[180:181], v[26:27], v[26:27], v[178:179] op_sel_hi:[1,1,0]
	v_mul_f32_e32 v178, v28, v28
	v_pk_fma_f32 v[184:185], v[28:29], v[28:29], v[178:179] op_sel_hi:[1,1,0]
	v_mul_f32_e32 v180, v30, v30
	v_mul_f32_e32 v184, v31, v31
	v_mul_f32_e32 v182, v32, v32
	v_mul_f32_e32 v178, v33, v33
	v_pk_add_f32 v[180:181], v[180:181], v[184:185]
	v_pk_add_f32 v[178:179], v[182:183], v[178:179]
	s_nop 0
	v_pk_add_f32 v[178:179], v[180:181], v[178:179]
	s_nop 0
	v_add_f32_e32 v178, v178, v179
	s_nop 1
	v_add_f32_dpp v178, v178, v178 quad_perm:[1,0,3,2] row_mask:0xf bank_mask:0xf
	s_nop 1
	v_add_f32_dpp v178, v178, v178 quad_perm:[2,3,0,1] row_mask:0xf bank_mask:0xf
	s_nop 1
	v_add_f32_dpp v178, v178, v178 row_half_mirror row_mask:0xf bank_mask:0xf
	s_nop 1
	v_add_f32_dpp v178, v178, v178 row_ror:8 row_mask:0xf bank_mask:0xf
	v_mov_b32_e32 v179, v178
	s_nop 1
	v_permlane16_swap_b32_e32 v178, v179
	s_nop 0
	v_add_f32_e32 v178, v178, v179
	v_mov_b32_e32 v179, v178
	s_nop 1
	v_permlane32_swap_b32_e32 v178, v179
	s_nop 0
	v_add_f32_e32 v178, v178, v179
	v_fmamk_f32 v178, v178, 0x3a800000, v235
	v_rsq_f32_e32 v182, v178
	s_nop 0
	v_pk_mul_f32 v[18:19], v[18:19], v[182:183] op_sel_hi:[1,0]
	v_pk_mul_f32 v[20:21], v[20:21], v[182:183] op_sel_hi:[1,0]
	v_pk_mul_f32 v[22:23], v[22:23], v[182:183] op_sel_hi:[1,0]
	v_pk_mul_f32 v[24:25], v[24:25], v[182:183] op_sel_hi:[1,0]

	v_pk_mul_f32 v[178:179], v[36:37], v[20:21]
	v_pk_mul_f32 v[180:181], v[34:35], v[18:19]
	v_pk_mul_f32 v[18:19], v[32:33], v[182:183] op_sel_hi:[1,0]
	v_pk_mul_f32 v[26:27], v[26:27], v[182:183] op_sel_hi:[1,0]
	v_pk_mul_f32 v[184:185], v[28:29], v[182:183] op_sel_hi:[1,0]
	v_pk_mul_f32 v[186:187], v[30:31], v[182:183] op_sel_hi:[1,0]

	v_pk_mul_f32 v[28:29], v[40:41], v[24:25]
	v_pk_mul_f32 v[30:31], v[38:39], v[22:23]

	v_pk_mul_f32 v[22:23], v[48:49], v[18:19]
	v_max_f32_e64 v18, |v180|, |v181|
	v_max_f32_e64 v19, |v178|, |v179|
	v_pk_mul_f32 v[20:21], v[44:45], v[184:185]
	v_pk_mul_f32 v[24:25], v[42:43], v[26:27]
	v_max3_f32 v18, v18, 0, v19
	v_max_f32_e64 v19, |v30|, |v31|
	v_max_f32_e64 v32, |v28|, |v29|
	v_pk_mul_f32 v[26:27], v[46:47], v[186:187]
	v_max3_f32 v18, v18, v19, v32
	v_max_f32_e64 v19, |v24|, |v25|
	v_max_f32_e64 v32, |v20|, |v21|
	v_max3_f32 v18, v18, v19, v32
	v_max_f32_e64 v19, |v26|, |v27|
	v_max_f32_e64 v32, |v22|, |v23|
	v_max3_f32 v18, v18, v19, v32
	s_nop 1
	v_max_f32_dpp v18, v18, v18 quad_perm:[1,0,3,2] row_mask:0xf bank_mask:0xf
	s_nop 1
	v_max_f32_dpp v18, v18, v18 quad_perm:[2,3,0,1] row_mask:0xf bank_mask:0xf
	s_nop 1
	v_max_f32_dpp v18, v18, v18 row_half_mirror row_mask:0xf bank_mask:0xf
	s_nop 1
	v_max_f32_dpp v18, v18, v18 row_ror:8 row_mask:0xf bank_mask:0xf
	v_mov_b32_e32 v19, v18
	s_nop 1
	v_permlane16_swap_b32_e32 v18, v19
	s_nop 0
	v_max_f32_e32 v18, v18, v19
	v_mov_b32_e32 v19, v18
	s_nop 1
	v_permlane32_swap_b32_e32 v18, v19
	s_nop 0
	v_max_f32_e32 v18, v18, v19
	s_and_saveexec_b64 s[4:5], s[6:7]
	s_xor_b64 s[16:17], exec, s[4:5]
	s_add_u32 s38, s50, s20
	s_addc_u32 s39, s51, s21
	s_or_saveexec_b64 s[16:17], s[16:17]
	s_waitcnt lgkmcnt(0)
	v_max_f32_e32 v32, s72, v18
	v_mov_b64_e32 v[18:19], s[38:39]
	s_xor_b64 exec, exec, s[16:17]
	s_cbranch_execz .LBB0_76
	v_mul_f32_e32 v18, 0x3c010204, v32
	s_ashr_i32 s37, s36, 31
	global_store_dword v1, v18, s[26:27]
	v_mov_b64_e32 v[18:19], s[36:37]
.LBB0_76:
	s_or_b64 exec, exec, s[16:17]
	v_div_scale_f32 v33, s[4:5], v32, v32, s73
	v_rcp_f32_e32 v182, v33
	s_nop 0
	v_fma_f32 v183, -v33, v182, 1.0
	v_fmac_f32_e32 v182, v183, v182
	v_div_scale_f32 v183, vcc, s73, v32, s73
	v_mul_f32_e32 v184, v183, v182
	v_fma_f32 v185, -v33, v184, v183
	v_fmac_f32_e32 v184, v185, v182
	v_fma_f32 v33, -v33, v184, v183
	v_div_fmas_f32 v33, v33, v182, v184
	v_div_fixup_f32 v182, v33, v32, s73
	v_mul_f32_e32 v184, v181, v182
	v_mul_f32_e32 v185, v178, v182
	v_mul_f32_e32 v183, v180, v182
	v_mul_f32_e32 v186, v179, v182
	v_rndne_f32_e32 v184, v184
	v_rndne_f32_e32 v185, v185
	v_rndne_f32_e32 v183, v183
	v_cvt_i32_f32_e32 v184, v184
	v_cvt_i32_f32_e32 v185, v185
	v_rndne_f32_e32 v186, v186
	v_cvt_i32_f32_e32 v183, v183
	v_cvt_i32_f32_e32 v186, v186
	v_med3_i32 v184, v184, s84, v236
	v_med3_i32 v185, v185, s84, v236
	v_med3_i32 v183, v183, s84, v236
	v_med3_i32 v186, v186, s84, v236
	v_lshlrev_b32_e32 v184, 8, v184
	v_lshlrev_b32_e32 v185, 16, v185
	v_lshlrev_b64 v[32:33], 10, v[18:19]
	v_and_b32_e32 v184, 0xff00, v184
	v_and_b32_e32 v185, 0xff0000, v185
	v_perm_b32 v183, v186, v183, s60
	v_or3_b32 v183, v183, v184, v185
	v_lshl_add_u64 v[32:33], v[210:211], 0, v[32:33]
	v_mul_f32_e32 v184, v31, v182
	v_mul_f32_e32 v185, v28, v182
	global_store_dword v[32:33], v183, off
	v_mul_f32_e32 v183, v30, v182
	v_mul_f32_e32 v186, v29, v182
	v_rndne_f32_e32 v184, v184
	v_rndne_f32_e32 v185, v185
	v_rndne_f32_e32 v183, v183
	v_cvt_i32_f32_e32 v184, v184
	v_cvt_i32_f32_e32 v185, v185
	v_rndne_f32_e32 v186, v186
	v_cvt_i32_f32_e32 v183, v183
	v_cvt_i32_f32_e32 v186, v186
	v_med3_i32 v184, v184, s84, v236
	v_med3_i32 v185, v185, s84, v236
	v_med3_i32 v183, v183, s84, v236
	v_med3_i32 v186, v186, s84, v236
	v_lshlrev_b32_e32 v184, 8, v184
	v_lshlrev_b32_e32 v185, 16, v185
	v_and_b32_e32 v184, 0xff00, v184
	v_and_b32_e32 v185, 0xff0000, v185
	v_perm_b32 v183, v186, v183, s60
	v_or3_b32 v183, v183, v184, v185
	v_mul_f32_e32 v184, v25, v182
	v_mul_f32_e32 v185, v20, v182
	global_store_dword v[32:33], v183, off offset:256
	v_mul_f32_e32 v183, v24, v182
	v_mul_f32_e32 v186, v21, v182
	v_rndne_f32_e32 v184, v184
	v_rndne_f32_e32 v185, v185
	v_rndne_f32_e32 v183, v183
	v_cvt_i32_f32_e32 v184, v184
	v_cvt_i32_f32_e32 v185, v185
	v_rndne_f32_e32 v186, v186
	v_cvt_i32_f32_e32 v183, v183
	v_cvt_i32_f32_e32 v186, v186
	v_med3_i32 v184, v184, s84, v236
	v_med3_i32 v185, v185, s84, v236
	v_med3_i32 v183, v183, s84, v236
	v_med3_i32 v186, v186, s84, v236
	v_lshlrev_b32_e32 v184, 8, v184
	v_lshlrev_b32_e32 v185, 16, v185
	v_and_b32_e32 v184, 0xff00, v184
	v_and_b32_e32 v185, 0xff0000, v185
	v_perm_b32 v183, v186, v183, s60
	v_or3_b32 v183, v183, v184, v185
	v_mul_f32_e32 v184, v27, v182
	v_mul_f32_e32 v185, v22, v182
	global_store_dword v[32:33], v183, off offset:512
	v_mul_f32_e32 v183, v26, v182
	v_mul_f32_e32 v182, v23, v182
	v_rndne_f32_e32 v184, v184
	v_rndne_f32_e32 v185, v185
	v_rndne_f32_e32 v183, v183
	v_cvt_i32_f32_e32 v184, v184
	v_cvt_i32_f32_e32 v185, v185
	v_rndne_f32_e32 v182, v182
	v_cvt_i32_f32_e32 v183, v183
	v_cvt_i32_f32_e32 v182, v182
	v_med3_i32 v184, v184, s84, v236
	v_med3_i32 v185, v185, s84, v236
	v_med3_i32 v183, v183, s84, v236
	v_med3_i32 v182, v182, s84, v236
	v_lshlrev_b32_e32 v184, 8, v184
	v_lshlrev_b32_e32 v185, 16, v185
	v_and_b32_e32 v184, 0xff00, v184
	v_and_b32_e32 v185, 0xff0000, v185
	v_perm_b32 v182, v182, v183, s60
	v_or3_b32 v182, v182, v184, v185
	global_store_dword v[32:33], v182, off offset:768

	v_fma_f32 v32, v50, v180, 0

	v_fma_f32 v184, v58, v180, 0
	v_fmac_f32_e32 v32, v54, v181
	v_fma_f32 v33, v51, v180, 0

	v_fmac_f32_e32 v184, v62, v181
	v_fma_f32 v185, v59, v180, 0

	v_fmac_f32_e32 v32, v66, v178
	v_fmac_f32_e32 v33, v55, v181
	v_fma_f32 v182, v52, v180, 0

	v_fmac_f32_e32 v184, v74, v178
	v_fmac_f32_e32 v185, v63, v181
	v_fma_f32 v186, v60, v180, 0
	v_fmac_f32_e32 v32, v70, v179
	v_fmac_f32_e32 v33, v67, v178
	v_fmac_f32_e32 v182, v56, v181
	v_fma_f32 v183, v53, v180, 0

	v_fmac_f32_e32 v184, v78, v179
	v_fmac_f32_e32 v185, v75, v178
	v_fmac_f32_e32 v186, v64, v181
	v_fma_f32 v180, v61, v180, 0

	v_fmac_f32_e32 v32, v82, v30
	v_fmac_f32_e32 v33, v71, v179
	v_fmac_f32_e32 v182, v68, v178
	v_fmac_f32_e32 v183, v57, v181

	v_fmac_f32_e32 v184, v90, v30
	v_fmac_f32_e32 v185, v79, v179
	v_fmac_f32_e32 v186, v76, v178
	v_fmac_f32_e32 v180, v65, v181
	v_fmac_f32_e32 v32, v86, v31
	v_fmac_f32_e32 v33, v83, v30
	v_fmac_f32_e32 v182, v72, v179
	v_fmac_f32_e32 v183, v69, v178

	v_fmac_f32_e32 v184, v94, v31
	v_fmac_f32_e32 v185, v91, v30
	v_fmac_f32_e32 v186, v80, v179
	v_fmac_f32_e32 v180, v77, v178

	v_fmac_f32_e32 v32, v98, v28
	v_fmac_f32_e32 v33, v87, v31
	v_fmac_f32_e32 v182, v84, v30
	v_fmac_f32_e32 v183, v73, v179

	v_fmac_f32_e32 v184, v106, v28
	v_fmac_f32_e32 v185, v95, v31
	v_fmac_f32_e32 v186, v92, v30
	v_fmac_f32_e32 v180, v81, v179
	v_fmac_f32_e32 v32, v102, v29
	v_fmac_f32_e32 v33, v99, v28
	v_fmac_f32_e32 v182, v88, v31
	v_fmac_f32_e32 v183, v85, v30

	v_fmac_f32_e32 v184, v110, v29
	v_fmac_f32_e32 v185, v107, v28
	v_fmac_f32_e32 v186, v96, v31
	v_fmac_f32_e32 v180, v93, v30

	v_fmac_f32_e32 v32, v114, v24
	v_fmac_f32_e32 v33, v103, v29
	v_fmac_f32_e32 v182, v100, v28
	v_fmac_f32_e32 v183, v89, v31

	v_fmac_f32_e32 v184, v122, v24
	v_fmac_f32_e32 v185, v111, v29
	v_fmac_f32_e32 v186, v108, v28
	v_fmac_f32_e32 v180, v97, v31
	v_fmac_f32_e32 v32, v118, v25
	v_fmac_f32_e32 v33, v115, v24
	v_fmac_f32_e32 v182, v104, v29
	v_fmac_f32_e32 v183, v101, v28

	v_fmac_f32_e32 v184, v126, v25
	v_fmac_f32_e32 v185, v123, v24
	v_fmac_f32_e32 v186, v112, v29
	v_fmac_f32_e32 v180, v109, v28

	v_fmac_f32_e32 v32, v130, v20
	v_fmac_f32_e32 v33, v119, v25
	v_fmac_f32_e32 v182, v116, v24
	v_fmac_f32_e32 v183, v105, v29

	v_fmac_f32_e32 v184, v138, v20
	v_fmac_f32_e32 v185, v127, v25
	v_fmac_f32_e32 v186, v124, v24
	v_fmac_f32_e32 v180, v113, v29
	v_fmac_f32_e32 v32, v134, v21
	v_fmac_f32_e32 v33, v131, v20
	v_fmac_f32_e32 v182, v120, v25
	v_fmac_f32_e32 v183, v117, v24

	v_fmac_f32_e32 v184, v142, v21
	v_fmac_f32_e32 v185, v139, v20
	v_fmac_f32_e32 v186, v128, v25
	v_fmac_f32_e32 v180, v125, v24

	v_fmac_f32_e32 v32, v146, v26
	v_fmac_f32_e32 v33, v135, v21
	v_fmac_f32_e32 v182, v132, v20
	v_fmac_f32_e32 v183, v121, v25

	v_fmac_f32_e32 v184, v154, v26
	v_fmac_f32_e32 v185, v143, v21
	v_fmac_f32_e32 v186, v140, v20
	v_fmac_f32_e32 v180, v129, v25
	v_fmac_f32_e32 v32, v150, v27
	v_fmac_f32_e32 v33, v147, v26
	v_fmac_f32_e32 v182, v136, v21
	v_fmac_f32_e32 v183, v133, v20

	v_fmac_f32_e32 v184, v158, v27
	v_fmac_f32_e32 v185, v155, v26
	v_fmac_f32_e32 v186, v144, v21
	v_fmac_f32_e32 v180, v141, v20

	v_fmac_f32_e32 v32, v162, v22
	v_fmac_f32_e32 v33, v151, v27
	v_fmac_f32_e32 v182, v148, v26
	v_fmac_f32_e32 v183, v137, v21

	v_fmac_f32_e32 v184, v170, v22
	v_fmac_f32_e32 v185, v159, v27
	v_fmac_f32_e32 v186, v156, v26
	v_fmac_f32_e32 v180, v145, v21
	v_fmac_f32_e32 v32, v166, v23
	v_fmac_f32_e32 v33, v163, v22
	v_fmac_f32_e32 v182, v152, v27
	v_fmac_f32_e32 v183, v149, v26

	v_fmac_f32_e32 v184, v174, v23
	v_fmac_f32_e32 v185, v171, v22
	v_fmac_f32_e32 v186, v160, v27
	v_fmac_f32_e32 v180, v157, v26
	v_fmac_f32_e32 v33, v167, v23
	v_fmac_f32_e32 v182, v164, v22
	v_fmac_f32_e32 v183, v153, v27
	v_fmac_f32_e32 v185, v175, v23
	v_fmac_f32_e32 v186, v172, v22
	v_fmac_f32_e32 v180, v161, v27
	v_cndmask_b32_e64 v21, v32, v184, s[8:9]
	v_fmac_f32_e32 v182, v168, v23
	v_fmac_f32_e32 v183, v165, v22
	v_fmac_f32_e32 v186, v176, v23
	v_fmac_f32_e32 v180, v173, v22
	v_cndmask_b32_e64 v22, v33, v185, s[8:9]
	v_fmac_f32_e32 v183, v169, v23
	v_fmac_f32_e32 v180, v177, v23
	v_cndmask_b32_e64 v23, v182, v186, s[8:9]
	v_cndmask_b32_e64 v24, v183, v180, s[8:9]
	v_cndmask_b32_e64 v20, v184, v32, s[8:9]
	s_nop 1
	v_add_f32_dpp v20, v21, v20 row_shl:4 row_mask:0xf bank_mask:0x5
	s_nop 1
	v_add_f32_dpp v20, v21, v20 row_shr:4 row_mask:0xf bank_mask:0xa
	v_cndmask_b32_e64 v21, v185, v33, s[8:9]
	s_nop 1
	v_add_f32_dpp v21, v22, v21 row_shl:4 row_mask:0xf bank_mask:0x5
	s_nop 1
	v_add_f32_dpp v21, v22, v21 row_shr:4 row_mask:0xf bank_mask:0xa
	v_cndmask_b32_e64 v22, v186, v182, s[8:9]
	s_nop 1
	v_add_f32_dpp v22, v23, v22 row_shl:4 row_mask:0xf bank_mask:0x5
	s_nop 1
	v_add_f32_dpp v22, v23, v22 row_shr:4 row_mask:0xf bank_mask:0xa
	v_cndmask_b32_e64 v23, v180, v183, s[8:9]
	s_nop 1
	v_add_f32_dpp v23, v24, v23 row_shl:4 row_mask:0xf bank_mask:0x5
	s_nop 1
	v_add_f32_dpp v23, v24, v23 row_shr:4 row_mask:0xf bank_mask:0xa
	v_cndmask_b32_e64 v24, v22, v20, s[10:11]
	v_cndmask_b32_e64 v20, v20, v22, s[10:11]
	v_cndmask_b32_e64 v22, v23, v21, s[10:11]
	v_cndmask_b32_e64 v21, v21, v23, s[10:11]
	s_nop 1
	v_add_f32_dpp v20, v20, v24 quad_perm:[2,3,0,1] row_mask:0xf bank_mask:0xf
	v_add_f32_dpp v21, v21, v22 quad_perm:[2,3,0,1] row_mask:0xf bank_mask:0xf
	v_cndmask_b32_e64 v22, v21, v20, s[12:13]
	v_cndmask_b32_e64 v20, v20, v21, s[12:13]
	s_nop 1
	v_add_f32_dpp v20, v20, v22 quad_perm:[1,0,3,2] row_mask:0xf bank_mask:0xf
	s_nop 1
	v_add_f32_dpp v20, v20, v20 row_ror:8 row_mask:0xf bank_mask:0xf
	v_mov_b32_e32 v21, v20
	s_nop 1
	v_permlane16_swap_b32_e32 v20, v21
	s_nop 0
	v_add_f32_e32 v20, v20, v21
	v_mov_b32_e32 v21, v20
	s_nop 1
	v_permlane32_swap_b32_e32 v20, v21
	s_nop 0
	s_and_saveexec_b64 s[16:17], s[14:15]
	s_cbranch_execz .LBB0_59
	s_waitcnt lgkmcnt(0)
	v_add_f32_e32 v20, v20, v21

	v_lshlrev_b64 v[18:19], 5, v[18:19]
	v_lshl_add_u64 v[18:19], v[208:209], 0, v[18:19]

	v_add_f32_e32 v20, v20, v240
	v_min_f32_e32 v21, 0, v20
	v_mul_f32_e64 v20, |v20|, s66
	v_exp_f32_e32 v20, v20
	s_nop 0
	v_add_f32_e32 v20, 1.0, v20
	v_log_f32_e32 v20, v20
	s_nop 0
	v_fmac_f32_e32 v21, 0xbf317218, v20
	global_store_dword v[18:19], v21, off
	s_branch .LBB0_59
